# SSD scan: G-tile pieces that the causal / anti-causal decay mask zeroes entirely are not loaded (lanes switched off for the load)
# speedup vs baseline: 1.0043x; 1.0034x over previous
.LBB0_680:
	s_lshl_b32 s4, s47, 7
	s_cmpk_lt_i32 s47, 0x100
	s_cselect_b32 s5, s23, 0xffffff00
	s_cselect_b32 s6, s25, 0x80
	s_and_b32 s5, s5, s4
	s_and_b32 s4, s6, s4
	s_add_i32 s4, s5, s4
	v_add_u32_e32 v16, s4, v138
	v_add_u32_e32 v18, s4, v139
	v_ashrrev_i32_e32 v17, 31, v16
	v_ashrrev_i32_e32 v19, 31, v18
	v_lshlrev_b64 v[16:17], 11, v[16:17]
	v_lshlrev_b64 v[18:19], 11, v[18:19]
	v_lshl_add_u64 v[16:17], v[112:113], 0, v[16:17]
	v_lshl_add_u64 v[18:19], v[112:113], 0, v[18:19]
	s_lshl_b32 s5, s47, 1
	global_load_dwordx4 v[48:51], v[16:17], off
	global_load_dwordx4 v[52:55], v[18:19], off
	s_or_b32 s6, s5, s14
	v_add_u32_e32 v18, s4, v140
	s_ashr_i32 s7, s6, 31
	v_ashrrev_i32_e32 v19, 31, v18
	s_lshl_b64 s[6:7], s[6:7], 15
	v_lshlrev_b64 v[18:19], 11, v[18:19]
	v_lshl_add_u64 v[16:17], v[234:235], 0, s[6:7]
	v_lshl_add_u64 v[18:19], v[130:131], 0, v[18:19]
	global_load_dwordx4 v[56:59], v[18:19], off offset:1024
	global_load_dwordx4 v[60:63], v[18:19], off offset:1536
	v_lshl_add_u64 v[18:19], v[114:115], 1, v[16:17]
	v_lshrrev_b32_e32 v20, 4, v24
	v_and_b32_e32 v21, 15, v24
	v_lshlrev_b32_e32 v21, 3, v21
	v_sub_u32_e32 v20, v20, v21
	v_sub_u32_e32 v21, 7, v20
	v_cndmask_b32_e64 v20, v21, v20, s[42:43]
	s_cmp_lg_u64 s[42:43], 0
	s_cselect_b32 s5, -32, 32
	v_cmp_le_i32_e64 s[6:7], 0, v20
	s_and_saveexec_b64 s[10:11], s[6:7]
	global_load_dwordx4 v[64:67], v[18:19], off
	s_mov_b64 exec, s[10:11]
	v_add_u32_e32 v18, s4, v141
	v_ashrrev_i32_e32 v19, 31, v18
	v_lshlrev_b64 v[18:19], 11, v[18:19]
	v_lshl_add_u64 v[18:19], v[130:131], 0, v[18:19]
	global_load_dwordx4 v[68:71], v[18:19], off offset:1024
	global_load_dwordx4 v[72:75], v[18:19], off offset:1536
	v_lshl_add_u64 v[18:19], v[116:117], 1, v[16:17]
	v_cmp_le_i32_e64 s[6:7], s5, v20
	s_and_saveexec_b64 s[10:11], s[6:7]
	global_load_dwordx4 v[76:79], v[18:19], off
	s_mov_b64 exec, s[10:11]
	v_add_u32_e32 v18, s4, v142
	v_ashrrev_i32_e32 v19, 31, v18
	v_lshlrev_b64 v[18:19], 11, v[18:19]
	v_lshl_add_u64 v[18:19], v[130:131], 0, v[18:19]
	global_load_dwordx4 v[80:83], v[18:19], off offset:1024
	global_load_dwordx4 v[84:87], v[18:19], off offset:1536
	v_lshl_add_u64 v[18:19], v[118:119], 1, v[16:17]
	s_lshl_b32 s32, s5, 1
	v_cmp_le_i32_e64 s[6:7], s32, v20
	s_and_saveexec_b64 s[10:11], s[6:7]
	global_load_dwordx4 v[88:91], v[18:19], off
	s_mov_b64 exec, s[10:11]
	v_add_u32_e32 v18, s4, v143
	v_ashrrev_i32_e32 v19, 31, v18
	v_lshlrev_b64 v[18:19], 11, v[18:19]
	v_lshl_add_u64 v[18:19], v[130:131], 0, v[18:19]
	v_lshl_add_u64 v[16:17], v[120:121], 1, v[16:17]
	global_load_dwordx4 v[92:95], v[18:19], off offset:1024
	global_load_dwordx4 v[96:99], v[18:19], off offset:1536
	s_mul_i32 s32, s5, 3
	v_cmp_le_i32_e64 s[6:7], s32, v20
	s_and_saveexec_b64 s[10:11], s[6:7]
	global_load_dwordx4 v[100:103], v[16:17], off
	s_mov_b64 exec, s[10:11]
	s_and_b64 vcc, exec, s[44:45]
	s_cbranch_vccnz .LBB0_682
	v_or_b32_e32 v16, s4, v253
	v_ashrrev_i32_e32 v17, 31, v16
	v_lshlrev_b64 v[18:19], 6, v[16:17]
	v_or_b32_e32 v16, 1, v16
	v_ashrrev_i32_e32 v17, 31, v16
	v_lshlrev_b64 v[16:17], 6, v[16:17]
	v_lshl_add_u64 v[18:19], v[178:179], 0, v[18:19]
	v_lshl_add_u64 v[16:17], v[178:179], 0, v[16:17]
	global_load_dword v122, v[18:19], off
	global_load_dword v123, v[16:17], off
